# conversion split: 6144 more expert-weight items per layer are converted in the idle second round of the router GEMM phase instead of at the start of phase A
# speedup vs baseline: 1.0097x; 1.0016x over previous
; #define LAS __attribute__((address_space(3)))
; #define REP(k) for (int _rep = 0; _rep < (((PROBE_MASK >> (k)) & 1) ? 2 : 1); ++_rep)
; __device__ __forceinline__ void p_expert_weights(Frame& F, int l, int it0, int it1, int nw, int w) {
;     LAS float* scr = (LAS float*)(F.lds + F.wave * 16384);
;     constexpr int I1 = 16 * 8, I2 = 4 * 32, PER_E = 2 * I1 + I2;
;     for (int it = it0 + w; it < it1; it += nw) {
; __global__ void __launch_bounds__(NTHR, 2) mk_fwd(Args args) {
;     ...
;             REP(0) { p_expert_weights(F, l, (last || F.G != 256) ? 0 : XW_TAIL_G, XW_ITEMS, F.G * NWAVES, F.wg * NWAVES + F.wave); __syncthreads(); }
.Lpa_body:
	v_readlane_b32 s36, v252, 8
	v_readlane_b32 s37, v252, 9
	s_mov_b32 s20, s97
	v_readlane_b32 s38, v252, 10
	v_readlane_b32 s39, v252, 11
	s_mov_b64 s[2:3], s[36:37]
	s_waitcnt vmcnt(0)
	v_mbcnt_lo_u32_b32 v6, -1, 0
	v_mbcnt_hi_u32_b32 v6, -1, v6
	s_nop 0
	v_readlane_b32 s2, v255, 30
	v_readlane_b32 s3, v255, 31
	s_or_b64 s[2:3], s[12:13], s[2:3]
	s_and_b64 s[2:3], s[2:3], exec
	s_cselect_b32 s0, 0, 0x6600
	v_readlane_b32 s2, v254, 28
	s_add_i32 s0, s0, s2
	s_add_i32 s21, s0, s20
	s_cmp_eq_u32 s100, 1
	s_cselect_b32 s21, 0x10000, s21
	s_cmp_gt_i32 s21, 0xc17f
	s_cbranch_scc1 .LBB0_279
	s_lshl_b32 s0, s20, 14
	s_mov_b32 s31, s23
	s_add_i32 s0, s0, 0
	s_lshl_b64 s[2:3], s[30:31], 20
	s_lshl_b64 s[40:41], s[30:31], 27
	s_add_u32 s50, s38, 0x5900000
	s_addc_u32 s51, s39, 0
	s_add_u32 s52, s38, 0xda00000
	v_readlane_b32 s56, v252, 16
	s_addc_u32 s53, s39, 0
	v_readlane_b32 s57, v252, 17
	v_readlane_b32 s58, v252, 18
	v_readlane_b32 s59, v252, 19
	v_readlane_b32 s60, v252, 20
	v_readlane_b32 s61, v252, 21
	v_readlane_b32 s62, v252, 22
	v_readlane_b32 s63, v252, 23
	v_readlane_b32 s68, v252, 28
	v_lshlrev_b32_e32 v3, 5, v6
	v_readlane_b32 s69, v252, 29
	s_add_u32 s54, s68, s40
	v_readlane_b32 s56, v252, 0
	v_ashrrev_i32_e32 v7, 5, v6
	v_and_b32_e32 v0, 31, v6
	s_movk_i32 s4, 0x84
	v_ashrrev_i32_e32 v8, 1, v6
	v_and_b32_e32 v4, 32, v3
	s_addc_u32 s55, s69, s41
	v_readlane_b32 s58, v252, 2
	v_lshl_add_u32 v1, v0, 2, s0
	v_mul_lo_u32 v2, v7, s4
	v_mul_u32_u24_e32 v3, 0x84, v4
	v_lshlrev_b32_e32 v5, 2, v8
	v_readlane_b32 s57, v252, 1
	v_readlane_b32 s59, v252, 3
	v_readlane_b32 s60, v252, 4
	v_readlane_b32 s61, v252, 5
	s_add_u32 s56, s58, s2
	s_waitcnt lgkmcnt(0)
	v_add3_u32 v9, s0, v3, v5
	v_readlane_b32 s4, v255, 14
	v_add_u32_e32 v10, v1, v2
	s_addc_u32 s57, s59, s3
	v_mov_b32_e32 v5, v193
	s_lshl_b32 s58, s21, 5
	s_lshl_b32 s59, s4, 5
	s_lshl_b32 s60, s21, 1
	s_lshl_b32 s61, s4, 1
	v_lshlrev_b32_e32 v192, 2, v0
	v_add_u32_e32 v11, 0x400, v10
	v_add_u32_e32 v12, 0x800, v10
	v_add_u32_e32 v13, 0xc00, v10
	v_add_u32_e32 v14, 0x1000, v10
	v_add_u32_e32 v15, 0x1400, v10
	v_add_u32_e32 v16, 0x1800, v10
	v_add_u32_e32 v17, 0x1c00, v10
	v_add_u32_e32 v18, 0x400, v9
	v_add_u32_e32 v19, 0x800, v9
	v_add_u32_e32 v20, 0xc00, v9
	v_readlane_b32 s64, v252, 24
	v_readlane_b32 s65, v252, 25
	v_readlane_b32 s66, v252, 26
	v_readlane_b32 s67, v252, 27
	v_readlane_b32 s70, v252, 30
	v_readlane_b32 s71, v252, 31
	v_readlane_b32 s62, v252, 6
	v_readlane_b32 s63, v252, 7
	v_readlane_b32 s5, v255, 15
	s_branch .LBB0_272

; #define LAS __attribute__((address_space(3)))
; __device__ __forceinline__ void p_expert_weights(Frame& F, int l, int it0, int it1, int nw, int w) {
;     LAS float* scr = (LAS float*)(F.lds + F.wave * 16384);
;     constexpr int I1 = 16 * 8, I2 = 4 * 32, PER_E = 2 * I1 + I2;
;     for (int it = it0 + w; it < it1; it += nw) {
; __global__ void __launch_bounds__(NTHR, 2) mk_fwd(Args args) {
;     ...
;             if (!last && F.G == 256 && F.wg >= 16) { __syncthreads(); FRESH(); p_expert_weights(F, l, XW_TAIL_E, XW_TAIL_G, 240 * NWAVES, (F.wg - 16) * NWAVES + F.wave); }
.LBB0_853:
	v_readlane_b32 s2, v255, 30
	v_readlane_b32 s3, v255, 31
	v_readlane_b32 s4, v254, 21
	s_xor_b64 s[2:3], s[2:3], -1
	v_readlane_b32 s5, v254, 22
	s_and_b64 s[2:3], s[2:3], s[4:5]
	v_readlane_b32 s4, v254, 26
	v_readlane_b32 s5, v254, 27
	s_and_b64 s[2:3], s[4:5], s[2:3]
	s_andn2_b64 vcc, exec, s[2:3]
	s_cbranch_vccnz .LBB0_861
	v_readlane_b32 s36, v252, 8
	v_readlane_b32 s37, v252, 9
	v_readlane_b32 s38, v252, 10
	v_readlane_b32 s39, v252, 11
	s_mov_b32 s0, s97
	s_mov_b64 s[2:3], s[38:39]
	s_mov_b64 s[4:5], s[36:37]
	s_waitcnt vmcnt(0) lgkmcnt(0)
	s_barrier
	v_mbcnt_lo_u32_b32 v0, -1, 0
	v_mbcnt_hi_u32_b32 v0, -1, v0
	s_nop 0
	v_readlane_b32 s4, v254, 29
	s_add_i32 s4, s4, s0
	s_cmpk_gt_i32 s4, 0x35ff
	s_cbranch_scc1 .LBB0_861
	s_lshl_b32 s0, s0, 14
	s_add_i32 s0, s0, 0
	s_add_i32 s38, s4, 0x3000
	s_lshl_b32 s18, s30, 27
	s_add_u32 s19, s2, 0xda00000
	v_readlane_b32 s40, v252, 16
	s_addc_u32 s39, s3, 0
	v_readlane_b32 s52, v252, 28
	v_readlane_b32 s41, v252, 17
	v_readlane_b32 s53, v252, 29
	s_add_u32 s40, s52, s18
	v_ashrrev_i32_e32 v5, 5, v0
	v_and_b32_e32 v4, 31, v0
	v_ashrrev_i32_e32 v8, 1, v0
	v_lshlrev_b32_e32 v0, 5, v0
	v_readlane_b32 s42, v252, 18
	s_addc_u32 s41, s53, 0
	s_movk_i32 s4, 0x84
	v_and_b32_e32 v6, 32, v0
	v_readlane_b32 s43, v252, 19
	v_readlane_b32 s44, v252, 20
	v_readlane_b32 s45, v252, 21
	v_lshl_add_u32 v1, v4, 2, s0
	v_mul_lo_u32 v2, v5, s4
	v_mul_u32_u24_e32 v0, 0x84, v6
	v_lshlrev_b32_e32 v3, 2, v8
	s_add_u32 s42, s2, 0x5900000
	v_add3_u32 v9, s0, v0, v3
	v_mov_b32_e32 v7, v193
	s_addc_u32 s43, s3, 0
	s_lshl_b32 s44, s38, 5
	s_lshl_b32 s45, s38, 1
	v_add_u32_e32 v10, v1, v2
	v_readlane_b32 s46, v252, 22
	v_readlane_b32 s47, v252, 23
	v_readlane_b32 s48, v252, 24
	v_readlane_b32 s49, v252, 25
	v_readlane_b32 s50, v252, 26
	v_readlane_b32 s51, v252, 27
	v_readlane_b32 s54, v252, 30
	v_readlane_b32 s55, v252, 31
	s_branch .LBB0_857
.LBB0_856:
	s_add_i32 s0, s38, 0x780
	s_add_i32 s44, s44, 0xf000
	s_addk_i32 s45, 0xf00
	s_cmpk_lt_i32 s38, 0x5e80
	s_mov_b32 s38, s0
	s_cbranch_scc0 .LBB0_861
